# window/selected attention units: Q loads and first K/V tile DMA in flight together (one round trip less per unit)
# speedup vs baseline: 1.0035x; 1.0035x over previous
.LBB0_519:
	s_or_b64 exec, exec, s[2:3]
	s_waitcnt lgkmcnt(0)
	s_barrier
	ds_read_b32 v2, v1
	s_mov_b64 s[2:3], -1
	s_waitcnt lgkmcnt(0)
	v_cmp_le_i32_e32 vcc, s29, v2
	v_readfirstlane_b32 s6, v2
	s_cbranch_vccnz .LBB0_514
	s_add_i32 s2, s6, 0xfffffe00
	s_cmpk_gt_i32 s6, 0x1ff
	s_cselect_b32 s2, s2, s6
	s_ashr_i32 s3, s2, 31
	s_lshr_b32 s3, s3, 26
	v_mov_b32_e32 v10, v0
	s_add_i32 s3, s2, s3
	s_ashr_i32 s42, s3, 6
	v_readfirstlane_b32 s34, v10
	s_andn2_b32 s3, s3, 63
	s_ashr_i32 s31, s34, 6
	s_sub_i32 s6, 7, s42
	s_sub_i32 s12, s2, s3
	s_and_b32 s13, s31, 3
	s_and_b32 s2, s12, 3
	s_ashr_i32 s14, s34, 8
	s_lshl_b32 s3, s6, 8
	s_lshl_b32 s43, s13, 6
	s_ashr_i32 s10, s12, 2
	s_or_b32 s30, s43, s3
	s_lshl_b32 s2, s2, 7
	s_lshl_b32 s3, s14, 6
	s_ashr_i32 s11, s10, 31
	s_add_i32 s2, s3, s2
	s_ashr_i32 s3, s2, 31
	s_lshl_b64 s[8:9], s[10:11], 21
	v_and_b32_e32 v203, 31, v10
	s_add_u32 s15, s18, s8
	v_or_b32_e32 v2, s30, v203
	s_addc_u32 s16, s19, s9
	s_lshl_b64 s[8:9], s[2:3], 1
	v_or_b32_e32 v4, 32, v2
	s_add_u32 s2, s15, s8
	v_mov_b32_e32 v5, v3
	v_bfe_u32 v202, v10, 5, 1
	s_addc_u32 s3, s16, s9
	v_lshlrev_b64 v[4:5], 10, v[4:5]
	v_lshlrev_b64 v[6:7], 10, v[2:3]
	v_lshlrev_b32_e32 v2, 4, v202
	v_lshl_add_u64 v[4:5], s[2:3], 0, v[4:5]
	v_lshl_add_u64 v[6:7], s[2:3], 0, v[6:7]
	v_lshl_add_u64 v[4:5], v[4:5], 0, v[2:3]
	v_lshl_add_u64 v[6:7], v[6:7], 0, v[2:3]
	global_load_dwordx4 v[162:165], v[4:5], off offset:96
	global_load_dwordx4 v[166:169], v[4:5], off offset:64
	global_load_dwordx4 v[170:173], v[6:7], off offset:96
	global_load_dwordx4 v[174:177], v[6:7], off offset:64
	global_load_dwordx4 v[178:181], v[4:5], off offset:32
	global_load_dwordx4 v[182:185], v[4:5], off
	global_load_dwordx4 v[186:189], v[6:7], off offset:32
	global_load_dwordx4 v[190:193], v[6:7], off
	s_lshl_b32 s40, s6, 2
	s_add_i32 s2, s40, -8
	s_cmp_gt_u32 s6, 2
	s_cselect_b32 s6, s2, 0
	s_lshl_b32 s12, s12, 6
	s_lshl_b64 s[2:3], s[10:11], 19
	s_and_b32 s12, s12, 0x80
	v_lshlrev_b32_e32 v6, 6, v10
	s_or_b32 s2, s2, s12
	v_and_b32_e32 v6, 0xf00, v6
	s_add_u32 s12, s20, s2
	v_and_b32_e32 v205, 63, v10
	v_lshl_or_b32 v6, s13, 12, v6
	s_addc_u32 s13, s21, s3
	v_mov_b32_e32 v5, v3
	v_lshlrev_b32_e32 v4, 8, v205
	s_add_u32 s2, s22, s2
	v_mov_b32_e32 v7, v3
	v_lshlrev_b32_e32 v204, 3, v10
	v_lshl_add_u64 v[4:5], s[12:13], 0, v[4:5]
	s_addc_u32 s3, s23, s3
	s_lshl_b32 s12, s31, 3
	s_lshl_b32 s14, s14, 5
	v_and_b32_e32 v15, 24, v204
	s_lshl_b32 s33, s31, 10
	s_ashr_i32 s13, s12, 31
	v_lshl_add_u64 v[6:7], s[2:3], 0, v[6:7]
	s_ashr_i32 s15, s14, 31
	v_mov_b32_e32 v9, v3
	v_lshlrev_b32_e32 v8, 1, v15
	s_lshl_b64 s[16:17], s[6:7], 14
	s_add_i32 s33, s33, 0
	v_lshl_add_u64 v[194:195], s[12:13], 1, v[4:5]
	v_lshl_add_u64 v[4:5], s[14:15], 1, v[6:7]
	v_mov_b32_e32 v11, v3
	v_mov_b32_e32 v12, v3
	v_mov_b32_e32 v13, v3
	v_mov_b32_e32 v14, v3
	s_add_i32 s2, s33, 0x8000
	v_lshl_add_u64 v[196:197], v[4:5], 0, v[8:9]
	v_lshl_add_u64 v[4:5], v[194:195], 0, s[16:17]
	s_mov_b32 m0, s33
	v_lshl_add_u64 v[6:7], v[196:197], 0, s[16:17]
	v_lshlrev_b32_e32 v206, 2, v202
	s_lshl_b32 s41, s6, 6
	v_mov_b32_e32 v16, v3
	v_mov_b32_e32 v17, v3
	v_mov_b32_e32 v8, v3
	v_mov_b32_e32 v211, 0
	s_add_i32 s35, s30, 0xfffffe00
	s_add_i32 s38, s30, 0xfffffe1f
	s_add_i32 s39, s30, 0xfffffe3f
	s_or_b32 s40, s40, 3
	s_barrier
	global_load_lds_dwordx4 v[4:5], off
	s_mov_b32 m0, s2
	s_and_b32 s2, s34, 0x3fffffc0
	global_load_lds_dwordx4 v[6:7], off
	s_lshl_b32 s2, s2, 2
	s_add_i32 s2, s2, 0
	s_add_i32 s12, s2, 0x10400
	v_lshlrev_b32_e32 v4, 1, v10
	v_lshrrev_b32_e32 v5, 2, v10
	v_lshl_add_u32 v200, v203, 2, s12
	v_add_u32_e32 v199, s12, v2
	s_lshl_b32 s12, s42, 8
	v_and_b32_e32 v4, 32, v4
	v_and_or_b32 v5, v5, 3, v206
	s_sub_i32 s12, s43, s12
	v_lshlrev_b32_e32 v5, 6, v5
	v_add_u32_e32 v2, 0, v4
	s_addk_i32 s12, 0x700
	v_add3_u32 v208, v2, v5, v15
	v_or_b32_e32 v2, s12, v203
	s_waitcnt vmcnt(0)
	v_lshlrev_b32_e32 v6, 10, v202
	v_lshlrev_b32_e32 v7, 4, v203
	v_sub_u32_e32 v2, v2, v206
	v_add3_u32 v207, 0, v6, v7
	v_subrev_u32_e32 v209, s41, v2
	v_mov_b32_e32 v2, v3
	v_mov_b32_e32 v4, v3
	v_mov_b32_e32 v5, v3
	v_mov_b32_e32 v6, v3
	v_mov_b32_e32 v7, v3
	v_mov_b32_e32 v10, v3
	v_mov_b32_e32 v11, v3
	v_mov_b32_e32 v12, v3
	v_mov_b32_e32 v13, v3
	v_mov_b32_e32 v14, v3
	v_mov_b32_e32 v15, v3
	v_mov_b64_e32 v[64:65], v[16:17]
	v_mov_b64_e32 v[80:81], v[16:17]
	v_mov_b64_e32 v[32:33], v[16:17]
	v_mov_b64_e32 v[48:49], v[16:17]
	s_or_b32 s34, s30, 63
	v_cmp_gt_u32_e64 s[2:3], 32, v205
	v_mov_b64_e32 v[62:63], v[14:15]
	v_mov_b64_e32 v[60:61], v[12:13]
	v_mov_b64_e32 v[58:59], v[10:11]
	v_mov_b64_e32 v[56:57], v[8:9]
	v_mov_b64_e32 v[54:55], v[6:7]
	v_mov_b64_e32 v[52:53], v[4:5]
	v_mov_b64_e32 v[50:51], v[2:3]
	v_mov_b64_e32 v[78:79], v[14:15]
	v_mov_b64_e32 v[76:77], v[12:13]
	v_mov_b64_e32 v[74:75], v[10:11]
	v_mov_b64_e32 v[72:73], v[8:9]
	v_mov_b64_e32 v[70:71], v[6:7]
	v_mov_b64_e32 v[68:69], v[4:5]
	v_mov_b64_e32 v[66:67], v[2:3]
	v_mov_b64_e32 v[30:31], v[14:15]
	v_mov_b64_e32 v[28:29], v[12:13]
	v_mov_b64_e32 v[26:27], v[10:11]
	v_mov_b64_e32 v[24:25], v[8:9]
	v_mov_b64_e32 v[22:23], v[6:7]
	v_mov_b64_e32 v[20:21], v[4:5]
	v_mov_b64_e32 v[18:19], v[2:3]
	v_mov_b64_e32 v[46:47], v[14:15]
	v_mov_b64_e32 v[44:45], v[12:13]
	v_mov_b64_e32 v[42:43], v[10:11]
	v_mov_b64_e32 v[40:41], v[8:9]
	v_mov_b64_e32 v[38:39], v[6:7]
	v_mov_b64_e32 v[36:37], v[4:5]
	v_mov_b64_e32 v[34:35], v[2:3]
	v_mov_b32_e32 v210, 0
	v_mov_b32_e32 v212, 0
	v_mov_b32_e32 v201, 0
	s_mov_b32 s12, s6
	v_mov_b32_e32 v82, 0
	v_mov_b32_e32 v83, v211
	v_mov_b32_e32 v84, v211
	v_mov_b32_e32 v85, v211
	v_mov_b32_e32 v86, v211
	v_mov_b32_e32 v87, v211
	v_mov_b32_e32 v88, v211
	v_mov_b32_e32 v89, v211
	v_mov_b32_e32 v90, v211
	v_mov_b32_e32 v91, v211
	v_mov_b32_e32 v92, v211
	v_mov_b32_e32 v93, v211
	v_mov_b32_e32 v94, v211
	v_mov_b32_e32 v95, v211
	v_mov_b32_e32 v96, v211
	v_mov_b32_e32 v97, v211
	s_waitcnt vmcnt(0) lgkmcnt(0)
	s_barrier
	s_branch .LBB0_524

.LBB0_641:
	s_or_b64 exec, exec, s[2:3]
	s_waitcnt lgkmcnt(0)
	s_barrier
	ds_read_b32 v2, v172
	s_mov_b64 s[2:3], -1
	s_waitcnt lgkmcnt(0)
	v_cmp_le_i32_e32 vcc, s15, v2
	v_readfirstlane_b32 s6, v2
	s_cbranch_vccnz .LBB0_636
	s_add_i32 s2, s6, 0xfffffe00
	s_cmpk_gt_i32 s6, 0x1ff
	s_cselect_b32 s2, s2, s6
	s_ashr_i32 s3, s2, 31
	s_lshr_b32 s3, s3, 26
	s_add_i32 s3, s2, s3
	s_ashr_i32 s10, s3, 6
	s_andn2_b32 s3, s3, 63
	v_mov_b32_e32 v14, v0
	s_sub_i32 s11, s2, s3
	s_and_b32 s2, s11, 3
	v_readfirstlane_b32 s43, v14
	s_ashr_i32 s41, s43, 6
	s_sub_i32 s44, 7, s10
	s_ashr_i32 s45, s43, 8
	s_and_b32 s12, s41, 3
	s_lshl_b32 s2, s2, 1
	s_ashr_i32 s8, s11, 2
	s_add_i32 s33, s45, s2
	s_lshl_b32 s2, s44, 8
	s_lshl_b32 s54, s12, 6
	s_ashr_i32 s9, s8, 31
	s_or_b32 s42, s54, s2
	s_lshl_b32 s2, s33, 6
	s_ashr_i32 s3, s2, 31
	s_lshl_b64 s[6:7], s[8:9], 21
	v_and_b32_e32 v177, 31, v14
	s_add_u32 s13, s16, s6
	v_or_b32_e32 v162, s42, v177
	s_addc_u32 s46, s17, s7
	s_lshl_b64 s[6:7], s[2:3], 1
	v_or_b32_e32 v164, 32, v162
	s_add_u32 s2, s13, s6
	v_mov_b32_e32 v165, v163
	s_addc_u32 s3, s46, s7
	v_lshlrev_b64 v[2:3], 10, v[162:163]
	v_lshlrev_b64 v[6:7], 10, v[164:165]
	v_lshl_add_u64 v[2:3], s[2:3], 0, v[2:3]
	v_lshl_add_u64 v[6:7], s[2:3], 0, v[6:7]
	s_lshl_b32 s2, s8, 1
	s_bfe_u32 s11, s11, 0x10001
	s_or_b32 s2, s11, s2
	s_ashr_i32 s3, s2, 31
	v_bfe_u32 v176, v14, 5, 1
	s_lshl_b64 s[2:3], s[2:3], 13
	v_lshlrev_b32_e32 v4, 4, v176
	v_mov_b32_e32 v5, v163
	s_add_u32 s2, s18, s2
	v_lshl_add_u64 v[6:7], v[6:7], 0, v[4:5]
	s_addc_u32 s3, s19, s3
	v_lshl_add_u64 v[2:3], v[2:3], 0, v[4:5]
	v_lshl_add_u64 v[8:9], v[162:163], 2, s[2:3]
	global_load_dwordx4 v[130:133], v[6:7], off offset:96
	global_load_dwordx4 v[138:141], v[6:7], off offset:64
	global_load_dwordx4 v[134:137], v[2:3], off offset:96
	global_load_dwordx4 v[142:145], v[2:3], off offset:64
	global_load_dwordx4 v[146:149], v[6:7], off offset:32
	global_load_dwordx4 v[154:157], v[6:7], off
	global_load_dwordx4 v[150:153], v[2:3], off offset:32
	global_load_dwordx4 v[158:161], v[2:3], off
	global_load_dword v184, v[8:9], off
	global_load_dword v183, v[8:9], off offset:128
	v_lshlrev_b32_e32 v6, 6, v14
	v_and_b32_e32 v6, 0xf00, v6
	v_lshl_or_b32 v6, s12, 12, v6
	s_lshl_b64 s[12:13], s[8:9], 19
	s_lshl_b32 s11, s11, 7
	s_or_b32 s55, s12, s11
	s_add_u32 s2, s20, s55
	v_and_b32_e32 v180, 63, v14
	s_addc_u32 s3, s21, s13
	v_mov_b32_e32 v3, v163
	v_lshlrev_b32_e32 v2, 8, v180
	s_add_u32 s46, s22, s55
	v_lshl_add_u64 v[10:11], s[2:3], 0, v[2:3]
	s_addc_u32 s47, s23, s13
	s_lshl_b32 s2, s41, 3
	s_lshl_b32 s48, s45, 5
	v_mov_b32_e32 v7, v163
	v_lshlrev_b32_e32 v178, 3, v14
	s_lshl_b32 s45, s41, 10
	s_ashr_i32 s3, s2, 31
	s_ashr_i32 s49, s48, 31
	v_and_b32_e32 v16, 24, v178
	v_lshl_add_u64 v[12:13], s[46:47], 0, v[6:7]
	s_add_i32 s45, s45, 0
	s_lshl_b64 s[50:51], s[2:3], 1
	s_lshl_b64 s[52:53], s[48:49], 1
	v_mov_b32_e32 v15, v163
	v_mov_b32_e32 v9, v163
	v_lshlrev_b32_e32 v8, 1, v16
	s_add_i32 s2, s45, 0x8000
	v_lshl_add_u64 v[10:11], v[10:11], 0, s[50:51]
	v_lshl_add_u64 v[12:13], v[12:13], 0, s[52:53]
	s_mov_b32 m0, s45
	v_lshl_add_u64 v[8:9], v[12:13], 0, v[8:9]
	v_lshlrev_b32_e32 v179, 2, v176
	s_lshl_b32 s49, s10, 2
	s_lshl_b32 s10, s10, 8
	s_sub_i32 s10, s54, s10
	s_or_b32 s48, s42, 63
	s_sub_i32 s49, 31, s49
	s_addk_i32 s10, 0x700
	v_mov_b32_e32 v34, v163
	v_mov_b32_e32 v35, v163
	v_mov_b32_e32 v48, v163
	v_mov_b32_e32 v49, v163
	v_mov_b32_e32 v36, v163
	v_mov_b32_e32 v37, v163
	v_mov_b32_e32 v38, v163
	v_mov_b32_e32 v39, v163
	s_barrier
	global_load_lds_dwordx4 v[10:11], off
	s_mov_b32 m0, s2
	s_and_b32 s2, s43, 0x3fffffc0
	global_load_lds_dwordx4 v[8:9], off
	s_lshl_b32 s2, s2, 2
	s_add_i32 s2, s2, 0
	v_lshlrev_b32_e32 v5, 1, v14
	v_lshrrev_b32_e32 v8, 2, v14
	s_add_i32 s43, s2, 0x10400
	v_and_b32_e32 v5, 32, v5
	v_and_or_b32 v8, v8, 3, v179
	v_lshlrev_b32_e32 v8, 6, v8
	v_lshl_add_u32 v174, v177, 2, s43
	v_add_u32_e32 v165, s43, v4
	s_or_b32 s43, s42, 32
	v_add_u32_e32 v4, 0, v5
	v_add3_u32 v182, v4, v8, v16
	v_or_b32_e32 v4, s10, v177
	s_add_u32 s10, s34, s50
	s_addc_u32 s50, s35, s51
	s_add_u32 s10, s10, s11
	s_addc_u32 s11, s50, 0
	s_add_u32 s10, s10, s12
	s_addc_u32 s11, s11, s13
	v_lshl_add_u64 v[166:167], s[10:11], 0, v[2:3]
	s_add_u32 s10, s52, s55
	v_and_b32_e32 v2, 3, v14
	s_addc_u32 s11, s53, s13
	v_lshl_or_b32 v2, v2, 4, s10
	v_mov_b32_e32 v3, s11
	s_waitcnt vmcnt(0)
	v_lshlrev_b32_e32 v9, 10, v176
	v_lshlrev_b32_e32 v10, 4, v177
	v_lshl_add_u64 v[2:3], v[2:3], 0, v[6:7]
	v_add3_u32 v185, 0, v9, v10
	v_sub_u32_e32 v188, v4, v179
	v_lshl_add_u64 v[168:169], s[4:5], 0, v[2:3]
	v_mov_b32_e32 v40, v163
	v_mov_b32_e32 v41, v163
	v_mov_b32_e32 v42, v163
	v_mov_b32_e32 v43, v163
	v_mov_b32_e32 v44, v163
	v_mov_b32_e32 v45, v163
	v_mov_b32_e32 v46, v163
	v_mov_b32_e32 v47, v163
	v_mov_b64_e32 v[64:65], v[48:49]
	v_mov_b64_e32 v[2:3], v[34:35]
	v_mov_b64_e32 v[18:19], v[34:35]
	s_mov_b32 s46, 63
	s_mov_b32 s47, 0
	v_or_b32_e32 v186, v184, v183
	v_cmp_gt_u32_e64 s[2:3], 32, v180
	v_mov_b32_e32 v189, 0
	s_mov_b64 s[10:11], 0
	v_mov_b64_e32 v[62:63], v[46:47]
	v_mov_b64_e32 v[60:61], v[44:45]
	v_mov_b64_e32 v[58:59], v[42:43]
	v_mov_b64_e32 v[56:57], v[40:41]
	v_mov_b64_e32 v[54:55], v[38:39]
	v_mov_b64_e32 v[52:53], v[36:37]
	v_mov_b64_e32 v[50:51], v[34:35]
	v_mov_b64_e32 v[4:5], v[36:37]
	v_mov_b64_e32 v[6:7], v[38:39]
	v_mov_b64_e32 v[8:9], v[40:41]
	v_mov_b64_e32 v[10:11], v[42:43]
	v_mov_b64_e32 v[12:13], v[44:45]
	v_mov_b64_e32 v[14:15], v[46:47]
	v_mov_b64_e32 v[16:17], v[48:49]
	v_mov_b64_e32 v[20:21], v[36:37]
	v_mov_b64_e32 v[22:23], v[38:39]
	v_mov_b64_e32 v[24:25], v[40:41]
	v_mov_b64_e32 v[26:27], v[42:43]
	v_mov_b64_e32 v[28:29], v[44:45]
	v_mov_b64_e32 v[30:31], v[46:47]
	v_mov_b64_e32 v[32:33], v[48:49]
	v_mov_b32_e32 v181, 0
	v_mov_b32_e32 v187, 0
	v_mov_b32_e32 v175, 0
	s_waitcnt vmcnt(0) lgkmcnt(0)
	s_barrier
	s_branch .LBB0_646
